# baseline (speedup 1.0000x reference)
.LBB1_7:
	v_readfirstlane_b32 s0, v0
	s_lshr_b32 s15, s0, 6
	s_add_i32 s0, s33, s28
	s_lshr_b32 s1, s0, 31
	s_ashr_i32 s0, s0, 2
	s_lshl_b32 s31, s2, 2
	s_add_i32 s0, s0, s1
	s_add_i32 s0, s0, s31
	s_ashr_i32 s1, s0, 31
	s_lshl_b64 s[0:1], s[0:1], 18
	s_waitcnt lgkmcnt(0)
	s_add_u32 s16, s6, s0
	s_addc_u32 s17, s7, s1
	s_lshl_b32 s15, s15, 10
	s_add_u32 s16, s16, s15
	s_addc_u32 s17, s17, 0
	s_add_u32 s0, s8, s0
	s_addc_u32 s1, s9, s1
	s_add_u32 s0, s0, s15
	s_addc_u32 s1, s1, 0
	s_add_i32 s18, s15, 0x14800
	v_and_b32_e32 v2, 0x3f0, v1
	s_mov_b32 m0, s18
	s_nop 0
	global_load_lds_dwordx4 v2, s[16:17]
	s_add_i32 s18, s15, 0x1a800
	s_mov_b32 m0, s18
	s_nop 0
	global_load_lds_dwordx4 v2, s[0:1]
	s_add_u32 s0, s16, 0x2000
	s_addc_u32 s1, s17, 0
	s_add_i32 s18, s15, 0x16800
	s_mov_b32 m0, s18
	s_nop 0
	global_load_lds_dwordx4 v2, s[0:1]
	s_add_u32 s0, s16, 0x4000
	s_addc_u32 s1, s17, 0
	s_add_i32 s15, s15, 0x18800
	s_mov_b32 m0, s15
	s_nop 0
	global_load_lds_dwordx4 v2, s[0:1]
	v_mov_b32_e32 v4, v1
	s_mov_b32 s36, s28
.LBB1_8:
	s_mul_hi_i32 s0, s3, 0x92492493
	s_add_i32 s0, s0, s3
	v_readfirstlane_b32 s15, v0
	s_lshr_b32 s1, s0, 31
	s_ashr_i32 s0, s0, 2
	s_lshr_b32 s34, s15, 6
	s_lshl_b32 s29, s2, 11
	s_add_i32 s2, s0, s1
	s_or_b32 s0, s14, s29
	s_lshl_b32 s37, s34, 5
	s_add_i32 s2, s2, s31
	s_add_i32 s35, s0, s37
	s_lshl_b32 s0, s3, 6
	s_ashr_i32 s3, s2, 31
	s_ashr_i32 s1, s0, 31
	s_lshl_b64 s[2:3], s[2:3], 18
	s_waitcnt lgkmcnt(0)
	s_add_u32 s16, s6, s2
	s_addc_u32 s17, s7, s3
	s_add_u32 s18, s8, s2
	s_addc_u32 s19, s9, s3
	s_and_b32 s2, s15, 0x3fffffc0
	s_lshl_b32 s38, s2, 2
	s_lshl_b32 s39, s34, 10
	s_add_u32 s2, s16, s39
	s_addc_u32 s3, s17, 0
	s_add_u32 s18, s18, s39
	s_addc_u32 s19, s19, 0
	s_add_i32 s16, s14, 0x100
	s_add_i32 s40, s39, 0x6000
	s_lshr_b32 s41, s16, 6
	s_mul_i32 s15, s35, 0xe00
	v_and_b32_e32 v208, 31, v0
	s_mul_hi_u32 s14, s35, 0xe00
	s_add_u32 s17, s4, s15
	v_bfe_u32 v196, v0, 5, 1
	s_addc_u32 s20, s5, s14
	s_lshl_b64 s[14:15], s[0:1], 1
	v_mul_u32_u24_e32 v1, 0x700, v208
	s_add_u32 s0, s17, s14
	v_lshl_or_b32 v190, v196, 3, v1
	s_addc_u32 s1, s20, s15
	v_mov_b32_e32 v3, 0
	v_lshlrev_b32_e32 v2, 1, v190
	v_lshl_add_u64 v[6:7], s[0:1], 0, v[2:3]
	global_load_dwordx4 v[142:145], v[6:7], off
	v_lshl_add_u64 v[8:9], v[6:7], 0, 32
	global_load_dwordx4 v[138:141], v[8:9], off
	v_lshl_add_u64 v[8:9], v[6:7], 0, 64
	global_load_dwordx4 v[130:133], v[8:9], off
	s_mov_b64 s[0:1], 0x60
	v_and_b32_e32 v195, 63, v0
	v_lshl_add_u64 v[6:7], v[6:7], 0, s[0:1]
	global_load_dwordx4 v[122:125], v[6:7], off
	v_lshlrev_b32_e32 v211, 4, v195
	s_mov_b32 m0, s39
	s_nop 0
	global_load_lds_dwordx4 v211, s[2:3]
	v_mov_b32_e32 v18, v3
	s_mov_b32 m0, s40
	s_nop 0
	global_load_lds_dwordx4 v211, s[18:19]
	s_add_u32 s0, s2, 0x2000
	s_addc_u32 s1, s3, 0
	s_add_i32 s17, s39, 0x2000
	s_mov_b32 m0, s17
	s_nop 0
	global_load_lds_dwordx4 v211, s[0:1]
	v_mov_b32_e32 v19, v3
	v_mov_b32_e32 v20, v3
	v_mov_b32_e32 v21, v3
	v_mov_b32_e32 v22, v3
	v_mov_b32_e32 v23, v3
	v_mov_b32_e32 v24, v3
	v_mov_b32_e32 v25, v3
	v_mov_b32_e32 v26, v3
	v_mov_b32_e32 v27, v3
	v_mov_b32_e32 v28, v3
	v_mov_b32_e32 v29, v3
	v_mov_b32_e32 v30, v3
	v_mov_b32_e32 v31, v3
	v_mov_b32_e32 v32, v3
	v_mov_b32_e32 v33, v3
	s_add_u32 s0, s2, 0x4000
	v_lshlrev_b32_e32 v193, 10, v196
	v_lshlrev_b32_e32 v194, 4, v208
	s_addc_u32 s1, s3, 0
	s_add_i32 s17, s39, 0x4000
	s_mov_b32 m0, s17
	s_nop 0
	global_load_lds_dwordx4 v211, s[0:1]
	v_or_b32_e32 v200, v193, v194
	s_waitcnt vmcnt(3) lgkmcnt(0)
	s_barrier
	ds_read_b128 v[6:9], v200
	s_waitcnt lgkmcnt(0)
	v_mfma_f32_32x32x16_f16 v[34:49], v[6:9], v[142:145], v[18:33]
	ds_read_b128 v[6:9], v200 offset:512
	s_add_u32 s0, s2, 0x6000
	s_addc_u32 s1, s3, 0
	v_lshlrev_b32_e32 v210, 2, v196
	v_lshlrev_b32_e32 v1, 1, v0
	v_lshlrev_b32_e32 v197, 3, v0
	v_and_b32_e32 v2, 0xc0, v4
	s_waitcnt lgkmcnt(0)
	v_mfma_f32_32x32x16_f16 v[18:33], v[6:9], v[142:145], v[18:33]
	ds_read_b128 v[6:9], v200 offset:2048
	v_and_b32_e32 v1, 32, v1
	v_and_b32_e32 v191, 24, v197
	v_lshl_or_b32 v192, v196, 8, v2
	v_mov_b32_e32 v2, v3
	v_mov_b32_e32 v4, v3
	v_mov_b32_e32 v5, v3
	s_waitcnt lgkmcnt(0)
	v_mfma_f32_32x32x16_f16 v[34:49], v[6:9], v[138:141], v[34:49]
	ds_read_b128 v[6:9], v200 offset:2560
	ds_read_b128 v[10:13], v200 offset:4608
	ds_read_b128 v[14:17], v200 offset:4096
	s_mov_b32 s20, 0
	s_mov_b32 s42, 3
	v_or3_b32 v209, v1, v191, v192
	s_movk_i32 s24, 0x2000
	s_movk_i32 s22, 0x4000
	v_lshl_or_b32 v198, v208, 2, s38
	s_waitcnt lgkmcnt(2)
	v_mfma_f32_32x32x16_f16 v[18:33], v[6:9], v[138:141], v[18:33]
	v_mov_b32_e32 v6, v3
	v_mov_b32_e32 v7, v3
	v_mov_b32_e32 v8, v3
	v_mov_b32_e32 v9, v3
	v_lshlrev_b32_e32 v212, 4, v196
	s_mov_b32 s23, 0x41000000
	v_mov_b32_e32 v203, v3
	s_waitcnt lgkmcnt(0)
	v_mfma_f32_32x32x16_f16 v[34:49], v[14:17], v[130:133], v[34:49]
	ds_read_b128 v[50:53], v200 offset:6656
	ds_read_b128 v[14:17], v200 offset:6144
	v_mfma_f32_32x32x16_f16 v[18:33], v[10:13], v[130:133], v[18:33]
	v_mov_b32_e32 v10, v3
	v_mov_b32_e32 v11, v3
	v_mov_b32_e32 v12, v3
	v_mov_b32_e32 v13, v3
	s_waitcnt lgkmcnt(0)
	v_mfma_f32_32x32x16_f16 v[34:49], v[14:17], v[122:125], v[34:49]
	v_mov_b32_e32 v16, v3
	v_mov_b32_e32 v17, v3
	v_mov_b32_e32 v14, v3
	v_mov_b32_e32 v15, v3
	v_mfma_f32_32x32x16_f16 v[18:33], v[50:53], v[122:125], v[18:33]
	s_nop 15
	s_nop 7
	s_nop 0
	v_max3_f32 v50, v34, v35, v18
	v_max3_f32 v51, v36, v37, v19
	s_nop 0
	v_max3_f32 v50, v50, v20, v21
	v_max3_f32 v51, v51, v40, v41
	s_nop 0
	v_max3_f32 v50, v50, v38, v39
	v_max3_f32 v51, v51, v24, v25
	s_nop 0
	v_max3_f32 v50, v50, v22, v23
	v_max3_f32 v51, v51, v44, v45
	s_nop 0
	v_max3_f32 v50, v50, v42, v43
	v_max3_f32 v51, v51, v28, v29
	s_nop 0
	v_max3_f32 v50, v50, v26, v27
	v_max3_f32 v51, v51, v48, v49
	s_nop 0
	v_max3_f32 v50, v50, v46, v47
	v_max3_f32 v51, v51, v32, v33
	s_nop 0
	v_max3_f32 v50, v50, v30, v31
	s_nop 0
	v_max_f32_e32 v50, v50, v51
	s_nop 0
	v_mov_b32_e32 v51, v50
	s_nop 1
	v_permlane32_swap_b32_e32 v50, v51
	v_max_f32_e32 v50, v50, v51
	s_nop 0
	v_add_f32_e32 v199, v3, v50
	v_sub_f32_e32 v51, v34, v50
	v_sub_f32_e32 v52, v35, v50
	v_sub_f32_e32 v53, v36, v50
	v_sub_f32_e32 v54, v37, v50
	v_sub_f32_e32 v55, v38, v50
	s_nop 0
	v_xor_b32_e32 v34, 0x80000000, v199
	v_sub_f32_e32 v56, v39, v50
	v_sub_f32_e32 v57, v40, v50
	v_sub_f32_e32 v58, v41, v50
	v_sub_f32_e32 v59, v42, v50
	v_sub_f32_e32 v60, v43, v50
	v_sub_f32_e32 v61, v44, v50
	v_sub_f32_e32 v62, v45, v50
	v_sub_f32_e32 v63, v46, v50
	v_sub_f32_e32 v64, v47, v50
	v_sub_f32_e32 v65, v48, v50
	v_sub_f32_e32 v81, v49, v50
	v_mov_b32_e32 v35, v34
	v_mov_b32_e32 v36, v34
	v_mov_b32_e32 v37, v34
	v_mov_b32_e32 v38, v34
	v_mov_b32_e32 v39, v34
	v_mov_b32_e32 v40, v34
	v_mov_b32_e32 v41, v34
	v_mov_b32_e32 v42, v34
	v_mov_b32_e32 v43, v34
	v_mov_b32_e32 v44, v34
	v_mov_b32_e32 v45, v34
	v_mov_b32_e32 v46, v34
	v_mov_b32_e32 v47, v34
	v_mov_b32_e32 v48, v34
	v_mov_b32_e32 v49, v34
	s_waitcnt vmcnt(0) lgkmcnt(0)
	s_barrier
	s_mov_b32 m0, s39
	s_nop 0
	global_load_lds_dwordx4 v211, s[0:1]
	s_add_u32 s0, s18, 0x2000
	s_addc_u32 s1, s19, 0
	s_add_i32 s17, s40, 0x2000
	s_mov_b32 m0, s17
	s_nop 0
	global_load_lds_dwordx4 v211, s[0:1]
	ds_read_b128 v[174:177], v200 offset:8192
	ds_read_b128 v[170:173], v200 offset:8704
	ds_read_b128 v[166:169], v200 offset:10240
	ds_read_b128 v[162:165], v200 offset:10752
	ds_read_b128 v[158:161], v200 offset:12288
	ds_read_b128 v[154:157], v200 offset:12800
	ds_read_b128 v[150:153], v200 offset:14336
	ds_read_b128 v[146:149], v200 offset:14848
	s_and_b32 s21, s16, 0xfc0
	v_sub_f32_e32 v18, v18, v50
	v_sub_f32_e32 v19, v19, v50
	v_sub_f32_e32 v20, v20, v50
	v_sub_f32_e32 v21, v21, v50
	v_sub_f32_e32 v22, v22, v50
	v_sub_f32_e32 v23, v23, v50
	v_sub_f32_e32 v24, v24, v50
	v_sub_f32_e32 v25, v25, v50
	v_sub_f32_e32 v26, v26, v50
	v_sub_f32_e32 v27, v27, v50
	v_sub_f32_e32 v28, v28, v50
	v_sub_f32_e32 v29, v29, v50
	v_sub_f32_e32 v30, v30, v50
	v_sub_f32_e32 v31, v31, v50
	v_sub_f32_e32 v32, v32, v50
	v_sub_f32_e32 v33, v33, v50
	v_exp_f32_e32 v66, v51
	v_exp_f32_e32 v67, v52
	v_exp_f32_e32 v68, v53
	v_exp_f32_e32 v69, v54
	v_exp_f32_e32 v70, v55
	v_exp_f32_e32 v71, v56
	v_exp_f32_e32 v72, v57
	v_exp_f32_e32 v73, v58
	v_exp_f32_e32 v74, v59
	v_exp_f32_e32 v75, v60
	v_exp_f32_e32 v76, v61
	v_exp_f32_e32 v77, v62
	v_exp_f32_e32 v78, v63
	v_exp_f32_e32 v79, v64
	v_exp_f32_e32 v80, v65
	v_exp_f32_e32 v81, v81
	v_exp_f32_e32 v50, v18
	v_exp_f32_e32 v51, v19
	v_exp_f32_e32 v52, v20
	v_exp_f32_e32 v53, v21
	v_exp_f32_e32 v54, v22
	v_exp_f32_e32 v55, v23
	v_exp_f32_e32 v56, v24
	v_exp_f32_e32 v57, v25
	v_exp_f32_e32 v58, v26
	v_exp_f32_e32 v59, v27
	v_exp_f32_e32 v60, v28
	v_exp_f32_e32 v61, v29
	v_exp_f32_e32 v62, v30
	v_exp_f32_e32 v63, v31
	v_exp_f32_e32 v64, v32
	v_exp_f32_e32 v65, v33
	s_add_u32 s16, s2, 0xa000
	s_waitcnt vmcnt(2) lgkmcnt(0)
	s_barrier
	s_addc_u32 s17, s3, 0
	v_subrev_u32_e32 v18, s21, v210
	s_add_u32 s18, s18, 0x4000
	v_add_u32_e32 v201, 0x1bb, v18
	v_mov_b64_e32 v[32:33], v[16:17]
	v_cmp_gt_u32_e64 s[0:1], 32, v195
	s_addc_u32 s19, s19, 0
	v_mov_b64_e32 v[30:31], v[14:15]
	v_mov_b64_e32 v[28:29], v[12:13]
	v_mov_b64_e32 v[26:27], v[10:11]
	v_mov_b64_e32 v[24:25], v[8:9]
	v_mov_b64_e32 v[22:23], v[6:7]
	v_mov_b64_e32 v[20:21], v[4:5]
	v_mov_b64_e32 v[18:19], v[2:3]
.LBB1_9:
	v_add_u32_e32 v182, s20, v209
	ds_read_b64_tr_b16 v[178:179], v182 offset:24576
	ds_read_b64_tr_b16 v[180:181], v182 offset:25088
	s_waitcnt lgkmcnt(9)
	v_mfma_f32_32x32x16_f16 v[98:113], v[174:177], v[142:145], v[34:49]
	v_add_f32_e32 v82, v66, v67
	v_add_f32_e32 v82, v68, v82
	v_add_f32_e32 v82, v69, v82
	v_add_f32_e32 v82, v70, v82
	v_add_f32_e32 v82, v71, v82
	v_cvt_pk_f16_f32 v134, v66, v67
	v_cvt_pk_f16_f32 v135, v68, v69
	ds_read_b64_tr_b16 v[174:175], v182 offset:28672
	ds_read_b64_tr_b16 v[176:177], v182 offset:29184
	v_add_f32_e32 v66, v72, v82
	s_waitcnt lgkmcnt(10)
	v_mfma_f32_32x32x16_f16 v[82:97], v[170:173], v[142:145], v[34:49]
	v_add_f32_e32 v66, v73, v66
	v_add_f32_e32 v66, v74, v66
	v_add_f32_e32 v66, v75, v66
	v_cvt_pk_f16_f32 v136, v70, v71
	v_cvt_pk_f16_f32 v137, v72, v73
	ds_read_b64_tr_b16 v[170:171], v182 offset:25600
	ds_read_b64_tr_b16 v[172:173], v182 offset:26112
	s_waitcnt lgkmcnt(11)
	v_mfma_f32_32x32x16_f16 v[98:113], v[166:169], v[138:141], v[98:113]
	v_add_f32_e32 v66, v76, v66
	v_add_f32_e32 v66, v77, v66
	v_add_f32_e32 v66, v78, v66
	v_add_f32_e32 v66, v79, v66
	v_cvt_pk_f16_f32 v126, v74, v75
	v_cvt_pk_f16_f32 v127, v76, v77
	ds_read_b64_tr_b16 v[74:75], v182 offset:29696
	ds_read_b64_tr_b16 v[76:77], v182 offset:30208
	s_waitcnt lgkmcnt(12)
	v_mfma_f32_32x32x16_f16 v[82:97], v[162:165], v[138:141], v[82:97]
	v_add_f32_e32 v66, v80, v66
	v_add_f32_e32 v66, v81, v66
	v_add_f32_e32 v66, v50, v66
	v_add_f32_e32 v66, v51, v66
	v_cvt_pk_f16_f32 v128, v78, v79
	v_cvt_pk_f16_f32 v129, v80, v81
	ds_read_b64_tr_b16 v[70:71], v182 offset:26624
	ds_read_b64_tr_b16 v[72:73], v182 offset:27136
	s_waitcnt lgkmcnt(13)
	v_mfma_f32_32x32x16_f16 v[98:113], v[158:161], v[130:133], v[98:113]
	v_add_f32_e32 v66, v52, v66
	v_add_f32_e32 v66, v53, v66
	v_add_f32_e32 v66, v54, v66
	v_add_f32_e32 v78, v55, v66
	v_cvt_pk_f16_f32 v118, v50, v51
	v_cvt_pk_f16_f32 v119, v52, v53
	ds_read_b64_tr_b16 v[66:67], v182 offset:30720
	ds_read_b64_tr_b16 v[68:69], v182 offset:31232
	s_waitcnt lgkmcnt(14)
	v_mfma_f32_32x32x16_f16 v[82:97], v[154:157], v[130:133], v[82:97]
	v_add_f32_e32 v50, v56, v78
	v_add_f32_e32 v50, v57, v50
	v_add_f32_e32 v50, v58, v50
	v_add_f32_e32 v50, v59, v50
	v_cvt_pk_f16_f32 v120, v54, v55
	v_cvt_pk_f16_f32 v121, v56, v57
	ds_read_b64_tr_b16 v[54:55], v182 offset:27648
	ds_read_b64_tr_b16 v[56:57], v182 offset:28160
	s_waitcnt lgkmcnt(14)
	v_mfma_f32_32x32x16_f16 v[98:113], v[150:153], v[122:125], v[98:113]
	v_add_f32_e32 v50, v60, v50
	v_add_f32_e32 v50, v61, v50
	v_add_f32_e32 v50, v62, v50
	v_add_f32_e32 v78, v63, v50
	v_cvt_pk_f16_f32 v114, v58, v59
	v_cvt_pk_f16_f32 v115, v60, v61
	ds_read_b64_tr_b16 v[50:51], v182 offset:31744
	ds_read_b64_tr_b16 v[52:53], v182 offset:32256
	v_mfma_f32_32x32x16_f16 v[82:97], v[146:149], v[122:125], v[82:97]
	v_add_f32_e32 v58, v64, v78
	v_add_f32_e32 v58, v65, v58
	v_cvt_pk_f16_f32 v116, v62, v63
	v_cvt_pk_f16_f32 v117, v64, v65
	v_max_f32_e32 v59, v98, v99
	v_max3_f32 v60, v100, v101, v102
	v_max3_f32 v59, v59, v103, v104
	v_max3_f32 v60, v60, v105, v106
	v_max3_f32 v59, v59, v107, v108
	v_max3_f32 v60, v60, v109, v110
	v_max3_f32 v59, v59, v111, v112
	v_add_f32_e32 v182, v203, v58
	v_max3_f32 v60, v60, v113, v82
	v_max3_f32 v59, v59, v83, v84
	v_max3_f32 v60, v60, v85, v86
	v_max3_f32 v59, v59, v87, v88
	v_max3_f32 v60, v60, v89, v90
	v_max3_f32 v59, v59, v91, v92
	v_max3_f32 v60, v60, v93, v94
	v_max3_f32 v59, v59, v95, v96
	v_max3_f32 v58, v59, v60, v97
	v_mov_b32_e32 v59, v58
	s_add_u32 s2, s16, 0xffffe000
	s_addc_u32 s3, s17, -1
	v_permlane32_swap_b32_e32 v58, v59
	s_add_i32 s20, s24, s39
	s_mov_b32 m0, s20
	v_max_f32_e32 v58, v58, v59
	global_load_lds_dwordx4 v211, s[2:3]
	s_add_i32 s2, s22, s40
	s_mov_b32 m0, s2
	v_cmp_lt_f32_e32 vcc, s23, v58
	global_load_lds_dwordx4 v211, s[18:19]
	s_cmp_lg_u64 vcc, 0
	s_cselect_b64 s[2:3], -1, 0
	s_cbranch_vccnz .LBB1_17

.LBB1_12:
	s_add_i32 s2, s22, 0x2000
	s_cmpk_lg_i32 s22, 0x4000
	s_cselect_b32 s43, s2, 0
	v_add_u32_e32 v183, s24, v209
	ds_read_b64_tr_b16 v[154:155], v183 offset:24576
	ds_read_b64_tr_b16 v[156:157], v183 offset:25088
	s_waitcnt lgkmcnt(9)
	v_mfma_f32_32x32x16_f16 v[66:81], v[58:61], v[142:145], v[34:49]
	v_add_f32_e32 v50, v98, v99
	v_add_f32_e32 v50, v100, v50
	v_add_f32_e32 v50, v101, v50
	v_add_f32_e32 v50, v102, v50
	v_add_f32_e32 v50, v103, v50
	v_cvt_pk_f16_f32 v134, v98, v99
	v_cvt_pk_f16_f32 v135, v100, v101
	ds_read_b64_tr_b16 v[150:151], v183 offset:28672
	ds_read_b64_tr_b16 v[152:153], v183 offset:29184
	v_add_f32_e32 v50, v104, v50
	v_add_f32_e32 v50, v105, v50
	v_add_f32_e32 v50, v106, v50
	v_add_f32_e32 v98, v107, v50
	s_waitcnt lgkmcnt(10)
	v_mfma_f32_32x32x16_f16 v[50:65], v[146:149], v[142:145], v[34:49]
	v_cvt_pk_f16_f32 v136, v102, v103
	v_cvt_pk_f16_f32 v137, v104, v105
	ds_read_b64_tr_b16 v[146:147], v183 offset:25600
	ds_read_b64_tr_b16 v[148:149], v183 offset:26112
	s_waitcnt lgkmcnt(11)
	v_mfma_f32_32x32x16_f16 v[66:81], v[178:181], v[138:141], v[66:81]
	v_add_f32_e32 v98, v108, v98
	v_add_f32_e32 v98, v109, v98
	v_add_f32_e32 v98, v110, v98
	v_add_f32_e32 v98, v111, v98
	v_cvt_pk_f16_f32 v126, v106, v107
	v_cvt_pk_f16_f32 v127, v108, v109
	ds_read_b64_tr_b16 v[106:107], v183 offset:29696
	ds_read_b64_tr_b16 v[108:109], v183 offset:30208
	s_waitcnt lgkmcnt(12)
	v_mfma_f32_32x32x16_f16 v[50:65], v[170:173], v[138:141], v[50:65]
	v_add_f32_e32 v98, v112, v98
	v_add_f32_e32 v98, v113, v98
	v_add_f32_e32 v98, v82, v98
	v_add_f32_e32 v98, v83, v98
	v_cvt_pk_f16_f32 v128, v110, v111
	v_cvt_pk_f16_f32 v129, v112, v113
	ds_read_b64_tr_b16 v[102:103], v183 offset:26624
	ds_read_b64_tr_b16 v[104:105], v183 offset:27136
	s_waitcnt lgkmcnt(13)
	v_mfma_f32_32x32x16_f16 v[66:81], v[174:177], v[130:133], v[66:81]
	v_add_f32_e32 v98, v84, v98
	v_add_f32_e32 v98, v85, v98
	v_add_f32_e32 v98, v86, v98
	v_add_f32_e32 v110, v87, v98
	v_cvt_pk_f16_f32 v118, v82, v83
	v_cvt_pk_f16_f32 v119, v84, v85
	ds_read_b64_tr_b16 v[98:99], v183 offset:30720
	ds_read_b64_tr_b16 v[100:101], v183 offset:31232
	s_waitcnt lgkmcnt(14)
	v_mfma_f32_32x32x16_f16 v[50:65], v[162:165], v[130:133], v[50:65]
	v_add_f32_e32 v82, v88, v110
	v_add_f32_e32 v82, v89, v82
	v_add_f32_e32 v82, v90, v82
	v_add_f32_e32 v82, v91, v82
	v_cvt_pk_f16_f32 v120, v86, v87
	v_cvt_pk_f16_f32 v121, v88, v89
	ds_read_b64_tr_b16 v[86:87], v183 offset:27648
	ds_read_b64_tr_b16 v[88:89], v183 offset:28160
	s_waitcnt lgkmcnt(14)
	v_mfma_f32_32x32x16_f16 v[66:81], v[166:169], v[122:125], v[66:81]
	v_add_f32_e32 v82, v92, v82
	v_add_f32_e32 v82, v93, v82
	v_add_f32_e32 v82, v94, v82
	v_add_f32_e32 v110, v95, v82
	v_cvt_pk_f16_f32 v114, v90, v91
	v_cvt_pk_f16_f32 v115, v92, v93
	ds_read_b64_tr_b16 v[82:83], v183 offset:31744
	ds_read_b64_tr_b16 v[84:85], v183 offset:32256
	v_mfma_f32_32x32x16_f16 v[50:65], v[158:161], v[122:125], v[50:65]
	v_add_f32_e32 v90, v96, v110
	v_add_f32_e32 v90, v97, v90
	v_cvt_pk_f16_f32 v116, v94, v95
	v_cvt_pk_f16_f32 v117, v96, v97
	v_max_f32_e32 v91, v66, v67
	v_max3_f32 v92, v68, v69, v70
	v_max3_f32 v91, v91, v71, v72
	v_max3_f32 v92, v92, v73, v74
	v_max3_f32 v91, v91, v75, v76
	v_max3_f32 v92, v92, v77, v78
	v_max3_f32 v91, v91, v79, v80
	v_add_f32_e32 v203, v182, v90
	v_max3_f32 v92, v92, v81, v50
	v_max3_f32 v91, v91, v51, v52
	v_max3_f32 v92, v92, v53, v54
	v_max3_f32 v91, v91, v55, v56
	v_max3_f32 v92, v92, v57, v58
	v_max3_f32 v91, v91, v59, v60
	v_max3_f32 v92, v92, v61, v62
	v_max3_f32 v91, v91, v63, v64
	v_max3_f32 v90, v91, v92, v65
	v_mov_b32_e32 v91, v90
	s_add_i32 s2, s22, s39
	s_mov_b32 m0, s2
	v_permlane32_swap_b32_e32 v90, v91
	global_load_lds_dwordx4 v211, s[16:17]
	s_add_u32 s2, s18, 0x2000
	s_addc_u32 s3, s19, 0
	s_add_i32 s20, s43, s40
	s_mov_b32 m0, s20
	v_max_f32_e32 v90, v90, v91
	global_load_lds_dwordx4 v211, s[2:3]
	v_cmp_lt_f32_e32 vcc, s23, v90
	s_cmp_lg_u64 vcc, 0
	s_cselect_b64 s[2:3], -1, 0
	s_cbranch_vccnz .LBB1_20

.Lsqk_0a:
	s_add_i32 s2, s24, 1
	s_cmp_ge_u32 s2, s41
	s_cselect_b64 s[20:21], -1, 0
	s_and_b64 vcc, exec, s[20:21]
	s_cbranch_vccnz .LBB1_27
	s_add_u32 s2, s16, 0xffffe000
	s_addc_u32 s3, s17, -1
	s_add_i32 s22, s43, s39
	s_mov_b32 m0, s22
	s_nop 0
	global_load_lds_dwordx4 v211, s[2:3]
.LBB1_27:
	s_add_i32 s25, s45, s24
	s_add_i32 s2, s44, s40
	s_add_i32 s3, s25, 2
	s_mov_b32 s51, s3
	s_cmp_lt_i32 s3, s50
	s_mov_b32 m0, s2
	s_nop 0
	global_load_lds_dwordx4 v211, s[18:19]
	s_cbranch_scc1 .LBB1_29
	s_cmp_gt_i32 s51, s50
	s_cbranch_scc1 .Lmfill_0a
	v_add_u32_e32 v60, 0xffffffa5, v201
	v_add_u32_e32 v59, 0xffffff85, v201
	v_cmp_le_i32_e32 vcc, v60, v204
	s_nop 1
	v_cndmask_b32_e32 v82, v205, v82, vcc
	v_cmp_lt_i32_e32 vcc, v59, v204
	s_nop 1
	v_cndmask_b32_e32 v99, v205, v99, vcc
	v_cmp_le_i32_e32 vcc, v59, v204
	v_add_u32_e32 v59, 0xffffffa6, v201
	s_nop 0
	v_cndmask_b32_e32 v98, v205, v98, vcc
	v_cmp_le_i32_e32 vcc, v59, v204
	v_add_u32_e32 v59, 0xffffff87, v201
	s_nop 0
	v_cndmask_b32_e32 v83, v205, v83, vcc
	v_cmp_le_i32_e32 vcc, v59, v204
	v_add_u32_e32 v59, 0xffffffa7, v201
	s_nop 0
	v_cndmask_b32_e32 v100, v205, v100, vcc
	v_cmp_le_i32_e32 vcc, v59, v204
	v_add_u32_e32 v59, 0xffffff88, v201
	s_nop 0
	v_cndmask_b32_e32 v84, v205, v84, vcc
	v_cmp_le_i32_e32 vcc, v59, v204
	v_add_u32_e32 v59, 0xffffffa8, v201
	s_nop 0
	v_cndmask_b32_e32 v101, v205, v101, vcc
	v_cmp_le_i32_e32 vcc, v59, v204
	v_add_u32_e32 v59, 0xffffff8d, v201
	s_nop 0
	v_cndmask_b32_e32 v85, v205, v85, vcc
	v_cmp_le_i32_e32 vcc, v59, v204
	v_add_u32_e32 v59, 0xffffffad, v201
	s_nop 0
	v_cndmask_b32_e32 v102, v205, v102, vcc
	v_cmp_le_i32_e32 vcc, v59, v204
	v_add_u32_e32 v59, 0xffffff8e, v201
	s_nop 0
	v_cndmask_b32_e32 v86, v205, v86, vcc
	v_cmp_le_i32_e32 vcc, v59, v204
	v_add_u32_e32 v59, 0xffffffae, v201
	s_nop 0
	v_cndmask_b32_e32 v103, v205, v103, vcc
	v_cmp_le_i32_e32 vcc, v59, v204
	v_add_u32_e32 v59, 0xffffff8f, v201
	s_nop 0
	v_cndmask_b32_e32 v87, v205, v87, vcc
	v_cmp_le_i32_e32 vcc, v59, v204
	v_add_u32_e32 v59, 0xffffffaf, v201
	s_nop 0
	v_cndmask_b32_e32 v104, v205, v104, vcc
	v_cmp_le_i32_e32 vcc, v59, v204
	v_add_u32_e32 v59, 0xffffff90, v201
	s_nop 0
	v_cndmask_b32_e32 v88, v205, v88, vcc
	v_cmp_le_i32_e32 vcc, v59, v204
	v_add_u32_e32 v59, 0xffffffb0, v201
	s_nop 0
	v_cndmask_b32_e32 v105, v205, v105, vcc
	v_cmp_le_i32_e32 vcc, v59, v204
	v_add_u32_e32 v59, 0xffffff95, v201
	s_nop 0
	v_cndmask_b32_e32 v89, v205, v89, vcc
	v_cmp_le_i32_e32 vcc, v59, v204
	v_add_u32_e32 v59, 0xffffffb5, v201
	s_nop 0
	v_cndmask_b32_e32 v106, v205, v106, vcc
	v_cmp_le_i32_e32 vcc, v59, v204
	v_add_u32_e32 v59, 0xffffff96, v201
	s_nop 0
	v_cndmask_b32_e32 v90, v205, v90, vcc
	v_cmp_le_i32_e32 vcc, v59, v204
	v_add_u32_e32 v59, 0xffffffb6, v201
	s_nop 0
	v_cndmask_b32_e32 v107, v205, v107, vcc
	v_cmp_le_i32_e32 vcc, v59, v204
	v_add_u32_e32 v59, 0xffffff97, v201
	s_nop 0
	v_cndmask_b32_e32 v91, v205, v91, vcc
	v_cmp_le_i32_e32 vcc, v59, v204
	v_add_u32_e32 v59, 0xffffffb7, v201
	s_nop 0
	v_cndmask_b32_e32 v108, v205, v108, vcc
	v_cmp_le_i32_e32 vcc, v59, v204
	v_add_u32_e32 v59, 0xffffff98, v201
	s_nop 0
	v_cndmask_b32_e32 v92, v205, v92, vcc
	v_cmp_le_i32_e32 vcc, v59, v204
	v_add_u32_e32 v59, 0xffffffb8, v201
	s_nop 0
	v_cndmask_b32_e32 v109, v205, v109, vcc
	v_cmp_le_i32_e32 vcc, v59, v204
	v_add_u32_e32 v59, 0xffffff9d, v201
	s_nop 0
	v_cndmask_b32_e32 v93, v205, v93, vcc
	v_cmp_le_i32_e32 vcc, v59, v204
	v_add_u32_e32 v59, 0xffffffbd, v201
	s_nop 0
	v_cndmask_b32_e32 v110, v205, v110, vcc
	v_cmp_le_i32_e32 vcc, v59, v204
	v_add_u32_e32 v59, 0xffffff9e, v201
	s_nop 0
	v_cndmask_b32_e32 v94, v205, v94, vcc
	v_cmp_le_i32_e32 vcc, v59, v204
	v_add_u32_e32 v59, 0xffffffbe, v201
	s_nop 0
	v_cndmask_b32_e32 v111, v205, v111, vcc
	v_cmp_le_i32_e32 vcc, v59, v204
	v_add_u32_e32 v59, 0xffffff9f, v201
	s_nop 0
	v_cndmask_b32_e32 v95, v205, v95, vcc
	v_cmp_le_i32_e32 vcc, v59, v204
	v_add_u32_e32 v59, 0xffffffbf, v201
	s_nop 0
	v_cndmask_b32_e32 v112, v205, v112, vcc
	v_cmp_le_i32_e32 vcc, v59, v204
	v_add_u32_e32 v59, 0xffffffa0, v201
	s_nop 0
	v_cndmask_b32_e32 v96, v205, v96, vcc
	v_cmp_le_i32_e32 vcc, v59, v204
	v_subrev_u32_e32 v59, 64, v201
	s_nop 0
	v_cndmask_b32_e32 v113, v205, v113, vcc
	v_cmp_le_i32_e32 vcc, v59, v204
	s_nop 1
	v_cndmask_b32_e32 v97, v205, v97, vcc

.Lsqk_0b:
	s_add_i32 s47, s24, 2
	s_cmp_ge_u32 s47, s41
	s_cselect_b64 s[22:23], -1, 0
	s_and_b64 vcc, exec, s[22:23]
	s_cbranch_vccnz .LBB1_36
	s_add_i32 s2, s44, s39
	s_mov_b32 m0, s2
	s_nop 0
	global_load_lds_dwordx4 v211, s[16:17]
.LBB1_36:
	s_add_i32 s2, s44, 0x2000
	s_cmpk_lg_i32 s44, 0x4000
	s_cselect_b32 s43, s2, 0
	s_cmp_lt_u32 s24, s41
	s_cselect_b64 s[26:27], -1, 0
	s_cmp_ge_u32 s24, s41
	s_cbranch_scc1 .LBB1_38
	s_add_u32 s2, s18, 0x2000
	s_addc_u32 s3, s19, 0
	s_add_i32 s24, s43, s40
	s_mov_b32 m0, s24
	s_nop 0
	global_load_lds_dwordx4 v211, s[2:3]

.LBB1_85:
	s_add_i32 s33, s33, s28
	s_lshr_b32 s5, s33, 31
	s_ashr_i32 s12, s33, 2
	s_add_i32 s5, s12, s5
	s_add_i32 s12, s5, s31
	s_ashr_i32 s13, s12, 31
	v_add3_u32 v0, v191, v1, v192
	s_lshl_b32 s20, s30, 8
	s_lshl_b64 s[12:13], s[12:13], 18
	v_or_b32_e32 v251, 0x1a800, v0
	v_max3_f32 v0, v18, v19, v2
	s_add_u32 s5, s6, s12
	v_max3_f32 v1, v20, v21, v3
	v_max3_f32 v0, v0, v4, v5
	s_addc_u32 s6, s7, s13
	v_max3_f32 v0, v0, v22, v23
	v_max3_f32 v1, v1, v24, v25
	s_add_u32 s7, s8, s12
	v_max3_f32 v0, v0, v6, v7
	v_max3_f32 v1, v1, v8, v9
	s_addc_u32 s8, s9, s13
	s_and_b32 s4, s4, 0x3fffffc0
	v_max3_f32 v0, v0, v26, v27
	v_max3_f32 v1, v1, v28, v29
	s_lshl_b32 s21, s4, 2
	s_lshl_b32 s23, s18, 10
	v_max3_f32 v0, v0, v10, v11
	v_max3_f32 v1, v1, v12, v13
	s_add_u32 s13, s5, s23
	v_max3_f32 v0, v0, v30, v31
	v_max3_f32 v1, v1, v32, v33
	s_addc_u32 s14, s6, 0
	v_max3_f32 v0, v0, v14, v15
	v_max3_f32 v1, v1, v16, v17
	s_add_u32 s15, s7, s23
	v_max_f32_e32 v0, v0, v1
	s_addc_u32 s16, s8, 0
	v_mov_b32_e32 v1, v0
	s_add_i32 s4, s20, 0x100
	s_nop 0
	v_permlane32_swap_b32_e32 v0, v1
	s_add_i32 s22, s23, 0x14800
	s_add_i32 s23, s23, 0x1a800
	s_lshr_b32 s24, s4, 6
	v_max_f32_e32 v0, v0, v1
	v_mov_b32_e32 v64, 0
	v_add_f32_e32 v249, v64, v0
	v_sub_f32_e32 v1, v18, v0
	v_sub_f32_e32 v18, v19, v0
	v_sub_f32_e32 v19, v20, v0
	v_sub_f32_e32 v20, v21, v0
	v_sub_f32_e32 v21, v22, v0
	v_sub_f32_e32 v22, v23, v0
	v_sub_f32_e32 v23, v24, v0
	v_sub_f32_e32 v24, v25, v0
	v_sub_f32_e32 v25, v26, v0
	v_sub_f32_e32 v26, v27, v0
	v_sub_f32_e32 v27, v28, v0
	v_sub_f32_e32 v28, v29, v0
	v_sub_f32_e32 v29, v30, v0
	v_sub_f32_e32 v30, v31, v0
	v_sub_f32_e32 v31, v32, v0
	s_nop 0
	v_xor_b32_e32 v32, 0x80000000, v249
	v_sub_f32_e32 v48, v33, v0
	v_mov_b32_e32 v33, v32
	v_mov_b32_e32 v34, v32
	v_mov_b32_e32 v35, v32
	v_mov_b32_e32 v36, v32
	v_mov_b32_e32 v37, v32
	v_mov_b32_e32 v38, v32
	v_mov_b32_e32 v39, v32
	v_mov_b32_e32 v40, v32
	v_mov_b32_e32 v41, v32
	v_mov_b32_e32 v42, v32
	v_mov_b32_e32 v43, v32
	v_mov_b32_e32 v44, v32
	v_mov_b32_e32 v45, v32
	v_mov_b32_e32 v46, v32
	v_mov_b32_e32 v47, v32
	s_add_u32 s4, s13, 0x6000
	s_waitcnt vmcnt(0) lgkmcnt(0)
	s_barrier
	s_addc_u32 s5, s14, 0
	s_mov_b32 m0, s22
	s_nop 0
	global_load_lds_dwordx4 v211, s[4:5]
	s_add_u32 s4, s15, 0x2000
	s_addc_u32 s5, s16, 0
	s_add_i32 s6, s23, 0x2000
	s_mov_b32 m0, s6
	s_nop 0
	global_load_lds_dwordx4 v211, s[4:5]
	ds_read_b128 v[188:191], v250 offset:8192
	ds_read_b128 v[184:187], v250 offset:8704
	ds_read_b128 v[180:183], v250 offset:10240
	ds_read_b128 v[176:179], v250 offset:10752
	ds_read_b128 v[172:175], v250 offset:12288
	ds_read_b128 v[168:171], v250 offset:12800
	ds_read_b128 v[164:167], v250 offset:14336
	ds_read_b128 v[160:163], v250 offset:14848
	v_sub_f32_e32 v2, v2, v0
	v_sub_f32_e32 v3, v3, v0
	v_sub_f32_e32 v4, v4, v0
	v_sub_f32_e32 v5, v5, v0
	v_sub_f32_e32 v6, v6, v0
	v_sub_f32_e32 v7, v7, v0
	v_sub_f32_e32 v8, v8, v0
	v_sub_f32_e32 v9, v9, v0
	v_sub_f32_e32 v10, v10, v0
	v_sub_f32_e32 v11, v11, v0
	v_sub_f32_e32 v12, v12, v0
	v_sub_f32_e32 v13, v13, v0
	v_sub_f32_e32 v14, v14, v0
	v_sub_f32_e32 v15, v15, v0
	v_sub_f32_e32 v16, v16, v0
	v_sub_f32_e32 v0, v17, v0
	v_exp_f32_e32 v80, v1
	v_exp_f32_e32 v81, v18
	v_exp_f32_e32 v82, v19
	v_exp_f32_e32 v83, v20
	v_exp_f32_e32 v84, v21
	v_exp_f32_e32 v85, v22
	v_exp_f32_e32 v86, v23
	v_exp_f32_e32 v87, v24
	v_exp_f32_e32 v88, v25
	v_exp_f32_e32 v89, v26
	v_exp_f32_e32 v90, v27
	v_exp_f32_e32 v91, v28
	v_exp_f32_e32 v92, v29
	v_exp_f32_e32 v93, v30
	v_exp_f32_e32 v94, v31
	v_exp_f32_e32 v95, v48
	v_exp_f32_e32 v48, v2
	v_exp_f32_e32 v49, v3
	v_exp_f32_e32 v50, v4
	v_exp_f32_e32 v51, v5
	v_exp_f32_e32 v52, v6
	v_exp_f32_e32 v53, v7
	v_exp_f32_e32 v54, v8
	v_exp_f32_e32 v55, v9
	v_exp_f32_e32 v56, v10
	v_exp_f32_e32 v57, v11
	v_exp_f32_e32 v58, v12
	v_exp_f32_e32 v59, v13
	v_exp_f32_e32 v60, v14
	v_exp_f32_e32 v61, v15
	v_exp_f32_e32 v62, v16
	v_exp_f32_e32 v63, v0
	s_waitcnt vmcnt(2) lgkmcnt(0)
	s_barrier
	s_mov_b32 s12, 0
	s_movk_i32 s25, 0x2000
	s_mov_b32 s6, 0
	s_mov_b32 s4, 1
	s_andn2_b64 vcc, exec, s[2:3]
	v_lshl_add_u32 v205, v208, 2, s21
	s_cbranch_vccnz .LBB1_101
	s_add_u32 s2, s15, 0x6000
	v_mov_b32_e32 v0, 0
	s_addc_u32 s3, s16, 0
	v_mov_b32_e32 v14, v0
	v_mov_b32_e32 v15, v0
	s_add_u32 s4, s13, 0xa000
	v_mov_b32_e32 v1, v0
	v_mov_b32_e32 v2, v0
	v_mov_b32_e32 v3, v0
	v_mov_b32_e32 v4, v0
	v_mov_b32_e32 v5, v0
	v_mov_b32_e32 v6, v0
	v_mov_b32_e32 v7, v0
	v_mov_b32_e32 v8, v0
	v_mov_b32_e32 v9, v0
	v_mov_b32_e32 v10, v0
	v_mov_b32_e32 v11, v0
	v_mov_b32_e32 v12, v0
	v_mov_b32_e32 v13, v0
	v_mov_b64_e32 v[30:31], v[14:15]
	s_addc_u32 s5, s14, 0
	s_movk_i32 s12, 0x4000
	s_movk_i32 s30, 0x2000
	s_mov_b32 s27, 6
	s_mov_b32 s17, 0x41000000
	v_mov_b64_e32 v[28:29], v[12:13]
	v_mov_b64_e32 v[26:27], v[10:11]
	v_mov_b64_e32 v[24:25], v[8:9]
	v_mov_b64_e32 v[22:23], v[6:7]
	v_mov_b64_e32 v[20:21], v[4:5]
	v_mov_b64_e32 v[18:19], v[2:3]
	v_mov_b64_e32 v[16:17], v[0:1]
	v_mov_b32_e32 v64, v0
.LBB1_87:
	v_add_u32_e32 v65, s6, v251
	ds_read_b64_tr_b16 v[192:193], v65
	ds_read_b64_tr_b16 v[194:195], v65 offset:512
	s_waitcnt lgkmcnt(9)
	v_mfma_f32_32x32x16_f16 v[112:127], v[188:191], v[140:143], v[32:47]
	v_add_f32_e32 v66, v80, v81
	v_add_f32_e32 v66, v82, v66
	v_add_f32_e32 v66, v83, v66
	v_add_f32_e32 v66, v84, v66
	v_add_f32_e32 v66, v85, v66
	v_cvt_pk_f16_f32 v156, v80, v81
	v_cvt_pk_f16_f32 v157, v82, v83
	ds_read_b64_tr_b16 v[188:189], v65 offset:4096
	ds_read_b64_tr_b16 v[190:191], v65 offset:4608
	s_waitcnt lgkmcnt(10)
	v_mfma_f32_32x32x16_f16 v[96:111], v[184:187], v[140:143], v[32:47]
	v_add_f32_e32 v66, v86, v66
	v_add_f32_e32 v66, v87, v66
	v_add_f32_e32 v66, v88, v66
	v_add_f32_e32 v66, v89, v66
	v_cvt_pk_f16_f32 v158, v84, v85
	v_cvt_pk_f16_f32 v159, v86, v87
	ds_read_b64_tr_b16 v[78:79], v65 offset:1024
	ds_read_b64_tr_b16 v[80:81], v65 offset:1536
	s_waitcnt lgkmcnt(11)
	v_mfma_f32_32x32x16_f16 v[112:127], v[180:183], v[136:139], v[112:127]
	v_add_f32_e32 v66, v90, v66
	v_add_f32_e32 v66, v91, v66
	v_add_f32_e32 v66, v92, v66
	v_add_f32_e32 v66, v93, v66
	v_cvt_pk_f16_f32 v152, v88, v89
	v_cvt_pk_f16_f32 v153, v90, v91
	ds_read_b64_tr_b16 v[74:75], v65 offset:5120
	ds_read_b64_tr_b16 v[76:77], v65 offset:5632
	s_waitcnt lgkmcnt(12)
	v_mfma_f32_32x32x16_f16 v[96:111], v[176:179], v[136:139], v[96:111]
	v_add_f32_e32 v66, v94, v66
	v_add_f32_e32 v66, v95, v66
	v_add_f32_e32 v66, v48, v66
	v_add_f32_e32 v66, v49, v66
	v_cvt_pk_f16_f32 v154, v92, v93
	v_cvt_pk_f16_f32 v155, v94, v95
	ds_read_b64_tr_b16 v[70:71], v65 offset:2048
	ds_read_b64_tr_b16 v[72:73], v65 offset:2560
	s_waitcnt lgkmcnt(13)
	v_mfma_f32_32x32x16_f16 v[112:127], v[172:175], v[132:135], v[112:127]
	v_add_f32_e32 v66, v50, v66
	v_add_f32_e32 v66, v51, v66
	v_add_f32_e32 v66, v52, v66
	v_add_f32_e32 v82, v53, v66
	v_cvt_pk_f16_f32 v148, v48, v49
	v_cvt_pk_f16_f32 v149, v50, v51
	ds_read_b64_tr_b16 v[66:67], v65 offset:6144
	ds_read_b64_tr_b16 v[68:69], v65 offset:6656
	s_waitcnt lgkmcnt(14)
	v_mfma_f32_32x32x16_f16 v[96:111], v[168:171], v[132:135], v[96:111]
	v_add_f32_e32 v48, v54, v82
	v_add_f32_e32 v48, v55, v48
	v_add_f32_e32 v48, v56, v48
	v_add_f32_e32 v48, v57, v48
	v_cvt_pk_f16_f32 v150, v52, v53
	v_cvt_pk_f16_f32 v151, v54, v55
	ds_read_b64_tr_b16 v[52:53], v65 offset:3072
	ds_read_b64_tr_b16 v[54:55], v65 offset:3584
	s_waitcnt lgkmcnt(14)
	v_mfma_f32_32x32x16_f16 v[112:127], v[164:167], v[128:131], v[112:127]
	v_add_f32_e32 v48, v58, v48
	v_add_f32_e32 v48, v59, v48
	v_add_f32_e32 v48, v60, v48
	v_add_f32_e32 v82, v61, v48
	v_cvt_pk_f16_f32 v144, v56, v57
	v_cvt_pk_f16_f32 v145, v58, v59
	ds_read_b64_tr_b16 v[48:49], v65 offset:7168
	ds_read_b64_tr_b16 v[50:51], v65 offset:7680
	v_mfma_f32_32x32x16_f16 v[96:111], v[160:163], v[128:131], v[96:111]
	v_add_f32_e32 v56, v62, v82
	v_add_f32_e32 v56, v63, v56
	v_cvt_pk_f16_f32 v146, v60, v61
	v_cvt_pk_f16_f32 v147, v62, v63
	v_max_f32_e32 v57, v112, v113
	v_max3_f32 v58, v114, v115, v116
	v_max3_f32 v57, v57, v117, v118
	v_max3_f32 v58, v58, v119, v120
	v_max3_f32 v57, v57, v121, v122
	v_max3_f32 v58, v58, v123, v124
	v_max3_f32 v57, v57, v125, v126
	v_add_f32_e32 v64, v64, v56
	v_max3_f32 v58, v58, v127, v96
	v_max3_f32 v57, v57, v97, v98
	v_max3_f32 v58, v58, v99, v100
	v_max3_f32 v57, v57, v101, v102
	v_max3_f32 v58, v58, v103, v104
	v_max3_f32 v57, v57, v105, v106
	v_max3_f32 v58, v58, v107, v108
	v_max3_f32 v57, v57, v109, v110
	v_max3_f32 v56, v57, v58, v111
	v_mov_b32_e32 v57, v56
	s_add_u32 s6, s4, 0xffffe000
	s_addc_u32 s7, s5, -1
	v_permlane32_swap_b32_e32 v56, v57
	s_add_i32 s8, s30, s22
	s_mov_b32 m0, s8
	v_max_f32_e32 v56, v56, v57
	global_load_lds_dwordx4 v211, s[6:7]
	s_add_u32 s6, s2, 0xffffe000
	s_addc_u32 s7, s3, -1
	s_add_i32 s8, s12, s23
	s_mov_b32 m0, s8
	v_cmp_lt_f32_e32 vcc, s17, v56
	global_load_lds_dwordx4 v211, s[6:7]
	s_cmp_lg_u64 vcc, 0
	s_cselect_b64 s[6:7], -1, 0
	s_cbranch_vccnz .LBB1_95

.LBB1_90:
	s_add_i32 s6, s12, 0x2000
	s_cmpk_lg_i32 s12, 0x4000
	s_cselect_b32 s25, s6, 0
	v_add_u32_e32 v65, s30, v251
	ds_read_b64_tr_b16 v[168:169], v65
	ds_read_b64_tr_b16 v[170:171], v65 offset:512
	s_waitcnt lgkmcnt(9)
	v_mfma_f32_32x32x16_f16 v[80:95], v[56:59], v[140:143], v[32:47]
	v_add_f32_e32 v48, v112, v113
	v_add_f32_e32 v48, v114, v48
	v_add_f32_e32 v48, v115, v48
	v_add_f32_e32 v48, v116, v48
	v_add_f32_e32 v48, v117, v48
	v_cvt_pk_f16_f32 v156, v112, v113
	v_cvt_pk_f16_f32 v157, v114, v115
	ds_read_b64_tr_b16 v[164:165], v65 offset:4096
	ds_read_b64_tr_b16 v[166:167], v65 offset:4608
	v_add_f32_e32 v48, v118, v48
	v_add_f32_e32 v48, v119, v48
	v_add_f32_e32 v48, v120, v48
	v_add_f32_e32 v66, v121, v48
	s_waitcnt lgkmcnt(10)
	v_mfma_f32_32x32x16_f16 v[48:63], v[160:163], v[140:143], v[32:47]
	v_cvt_pk_f16_f32 v158, v116, v117
	v_cvt_pk_f16_f32 v159, v118, v119
	ds_read_b64_tr_b16 v[160:161], v65 offset:1024
	ds_read_b64_tr_b16 v[162:163], v65 offset:1536
	s_waitcnt lgkmcnt(11)
	v_mfma_f32_32x32x16_f16 v[80:95], v[188:191], v[136:139], v[80:95]
	v_add_f32_e32 v66, v122, v66
	v_add_f32_e32 v66, v123, v66
	v_add_f32_e32 v66, v124, v66
	v_add_f32_e32 v66, v125, v66
	v_cvt_pk_f16_f32 v152, v120, v121
	v_cvt_pk_f16_f32 v153, v122, v123
	ds_read_b64_tr_b16 v[116:117], v65 offset:5120
	ds_read_b64_tr_b16 v[118:119], v65 offset:5632
	s_waitcnt lgkmcnt(12)
	v_mfma_f32_32x32x16_f16 v[48:63], v[184:187], v[136:139], v[48:63]
	v_add_f32_e32 v66, v126, v66
	v_add_f32_e32 v66, v127, v66
	v_add_f32_e32 v66, v96, v66
	v_add_f32_e32 v66, v97, v66
	v_cvt_pk_f16_f32 v154, v124, v125
	v_cvt_pk_f16_f32 v155, v126, v127
	ds_read_b64_tr_b16 v[112:113], v65 offset:2048
	ds_read_b64_tr_b16 v[114:115], v65 offset:2560
	s_waitcnt lgkmcnt(13)
	v_mfma_f32_32x32x16_f16 v[80:95], v[74:77], v[132:135], v[80:95]
	v_add_f32_e32 v66, v98, v66
	v_add_f32_e32 v66, v99, v66
	v_add_f32_e32 v66, v100, v66
	v_add_f32_e32 v66, v101, v66
	v_cvt_pk_f16_f32 v148, v96, v97
	v_cvt_pk_f16_f32 v149, v98, v99
	ds_read_b64_tr_b16 v[74:75], v65 offset:6144
	ds_read_b64_tr_b16 v[76:77], v65 offset:6656
	s_waitcnt lgkmcnt(14)
	v_mfma_f32_32x32x16_f16 v[48:63], v[176:179], v[132:135], v[48:63]
	v_add_f32_e32 v66, v102, v66
	v_add_f32_e32 v66, v103, v66
	v_add_f32_e32 v66, v104, v66
	v_add_f32_e32 v66, v105, v66
	v_cvt_pk_f16_f32 v150, v100, v101
	v_cvt_pk_f16_f32 v151, v102, v103
	ds_read_b64_tr_b16 v[70:71], v65 offset:3072
	ds_read_b64_tr_b16 v[72:73], v65 offset:3584
	s_waitcnt lgkmcnt(14)
	v_mfma_f32_32x32x16_f16 v[80:95], v[180:183], v[128:131], v[80:95]
	v_add_f32_e32 v66, v106, v66
	v_add_f32_e32 v66, v107, v66
	v_add_f32_e32 v66, v108, v66
	v_add_f32_e32 v78, v109, v66
	v_cvt_pk_f16_f32 v144, v104, v105
	v_cvt_pk_f16_f32 v145, v106, v107
	ds_read_b64_tr_b16 v[66:67], v65 offset:7168
	ds_read_b64_tr_b16 v[68:69], v65 offset:7680
	v_mfma_f32_32x32x16_f16 v[48:63], v[172:175], v[128:131], v[48:63]
	v_add_f32_e32 v65, v110, v78
	v_add_f32_e32 v65, v111, v65
	v_cvt_pk_f16_f32 v146, v108, v109
	v_cvt_pk_f16_f32 v147, v110, v111
	v_max_f32_e32 v78, v80, v81
	v_max3_f32 v79, v82, v83, v84
	v_max3_f32 v78, v78, v85, v86
	v_max3_f32 v79, v79, v87, v88
	v_max3_f32 v78, v78, v89, v90
	v_max3_f32 v79, v79, v91, v92
	v_max3_f32 v78, v78, v93, v94
	v_add_f32_e32 v64, v64, v65
	v_max3_f32 v79, v79, v95, v48
	v_max3_f32 v78, v78, v49, v50
	v_max3_f32 v79, v79, v51, v52
	v_max3_f32 v78, v78, v53, v54
	v_max3_f32 v79, v79, v55, v56
	v_max3_f32 v78, v78, v57, v58
	v_max3_f32 v79, v79, v59, v60
	v_max3_f32 v78, v78, v61, v62
	v_max3_f32 v65, v78, v79, v63
	v_mov_b32_e32 v78, v65
	s_add_i32 s6, s12, s22
	s_mov_b32 m0, s6
	v_permlane32_swap_b32_e32 v65, v78
	global_load_lds_dwordx4 v211, s[4:5]
	s_add_i32 s6, s25, s23
	s_mov_b32 m0, s6
	v_max_f32_e32 v65, v65, v78
	global_load_lds_dwordx4 v211, s[2:3]
	v_cmp_lt_f32_e32 vcc, s17, v65
	s_cmp_lg_u64 vcc, 0
	s_cselect_b64 s[6:7], -1, 0
	s_cbranch_vccnz .LBB1_98

.Lsqk_1a:
	s_add_i32 s2, s31, 1
	s_cmp_ge_u32 s2, s24
	s_cselect_b64 s[8:9], -1, 0
	s_and_b64 vcc, exec, s[8:9]
	s_cbranch_vccnz .LBB1_114
	s_add_u32 s2, s6, 0xffffe000
	s_addc_u32 s3, s7, -1
	s_add_i32 s12, s25, s22
	s_mov_b32 m0, s12
	s_nop 0
	global_load_lds_dwordx4 v211, s[2:3]
.LBB1_114:
	s_add_i32 s14, s27, s31
	s_add_i32 s2, s26, s23
	s_add_i32 s3, s14, 2
	s_mov_b32 s51, s3
	s_cmp_lt_i32 s3, s50
	s_mov_b32 m0, s2
	s_nop 0
	global_load_lds_dwordx4 v211, s[4:5]
	s_cbranch_scc1 .LBB1_116
	s_cmp_gt_i32 s51, s50
	s_cbranch_scc1 .Lmfill_1a
	v_add_u32_e32 v58, 0xffffffa5, v65
	v_add_u32_e32 v57, 0xffffff85, v65
	v_cmp_le_i32_e32 vcc, v58, v207
	s_nop 1
	v_cndmask_b32_e32 v96, v252, v96, vcc
	v_cmp_lt_i32_e32 vcc, v57, v207
	s_nop 1
	v_cndmask_b32_e32 v113, v252, v113, vcc
	v_cmp_le_i32_e32 vcc, v57, v207
	v_add_u32_e32 v57, 0xffffffa6, v65
	s_nop 0
	v_cndmask_b32_e32 v112, v252, v112, vcc
	v_cmp_le_i32_e32 vcc, v57, v207
	v_add_u32_e32 v57, 0xffffff87, v65
	s_nop 0
	v_cndmask_b32_e32 v97, v252, v97, vcc
	v_cmp_le_i32_e32 vcc, v57, v207
	v_add_u32_e32 v57, 0xffffffa7, v65
	s_nop 0
	v_cndmask_b32_e32 v114, v252, v114, vcc
	v_cmp_le_i32_e32 vcc, v57, v207
	v_add_u32_e32 v57, 0xffffff88, v65
	s_nop 0
	v_cndmask_b32_e32 v98, v252, v98, vcc
	v_cmp_le_i32_e32 vcc, v57, v207
	v_add_u32_e32 v57, 0xffffffa8, v65
	s_nop 0
	v_cndmask_b32_e32 v115, v252, v115, vcc
	v_cmp_le_i32_e32 vcc, v57, v207
	v_add_u32_e32 v57, 0xffffff8d, v65
	s_nop 0
	v_cndmask_b32_e32 v99, v252, v99, vcc
	v_cmp_le_i32_e32 vcc, v57, v207
	v_add_u32_e32 v57, 0xffffffad, v65
	s_nop 0
	v_cndmask_b32_e32 v116, v252, v116, vcc
	v_cmp_le_i32_e32 vcc, v57, v207
	v_add_u32_e32 v57, 0xffffff8e, v65
	s_nop 0
	v_cndmask_b32_e32 v100, v252, v100, vcc
	v_cmp_le_i32_e32 vcc, v57, v207
	v_add_u32_e32 v57, 0xffffffae, v65
	s_nop 0
	v_cndmask_b32_e32 v117, v252, v117, vcc
	v_cmp_le_i32_e32 vcc, v57, v207
	v_add_u32_e32 v57, 0xffffff8f, v65
	s_nop 0
	v_cndmask_b32_e32 v101, v252, v101, vcc
	v_cmp_le_i32_e32 vcc, v57, v207
	v_add_u32_e32 v57, 0xffffffaf, v65
	s_nop 0
	v_cndmask_b32_e32 v118, v252, v118, vcc
	v_cmp_le_i32_e32 vcc, v57, v207
	v_add_u32_e32 v57, 0xffffff90, v65
	s_nop 0
	v_cndmask_b32_e32 v102, v252, v102, vcc
	v_cmp_le_i32_e32 vcc, v57, v207
	v_add_u32_e32 v57, 0xffffffb0, v65
	s_nop 0
	v_cndmask_b32_e32 v119, v252, v119, vcc
	v_cmp_le_i32_e32 vcc, v57, v207
	v_add_u32_e32 v57, 0xffffff95, v65
	s_nop 0
	v_cndmask_b32_e32 v103, v252, v103, vcc
	v_cmp_le_i32_e32 vcc, v57, v207
	v_add_u32_e32 v57, 0xffffffb5, v65
	s_nop 0
	v_cndmask_b32_e32 v120, v252, v120, vcc
	v_cmp_le_i32_e32 vcc, v57, v207
	v_add_u32_e32 v57, 0xffffff96, v65
	s_nop 0
	v_cndmask_b32_e32 v104, v252, v104, vcc
	v_cmp_le_i32_e32 vcc, v57, v207
	v_add_u32_e32 v57, 0xffffffb6, v65
	s_nop 0
	v_cndmask_b32_e32 v121, v252, v121, vcc
	v_cmp_le_i32_e32 vcc, v57, v207
	v_add_u32_e32 v57, 0xffffff97, v65
	s_nop 0
	v_cndmask_b32_e32 v105, v252, v105, vcc
	v_cmp_le_i32_e32 vcc, v57, v207
	v_add_u32_e32 v57, 0xffffffb7, v65
	s_nop 0
	v_cndmask_b32_e32 v122, v252, v122, vcc
	v_cmp_le_i32_e32 vcc, v57, v207
	v_add_u32_e32 v57, 0xffffff98, v65
	s_nop 0
	v_cndmask_b32_e32 v106, v252, v106, vcc
	v_cmp_le_i32_e32 vcc, v57, v207
	v_add_u32_e32 v57, 0xffffffb8, v65
	s_nop 0
	v_cndmask_b32_e32 v123, v252, v123, vcc
	v_cmp_le_i32_e32 vcc, v57, v207
	v_add_u32_e32 v57, 0xffffff9d, v65
	s_nop 0
	v_cndmask_b32_e32 v107, v252, v107, vcc
	v_cmp_le_i32_e32 vcc, v57, v207
	v_add_u32_e32 v57, 0xffffffbd, v65
	s_nop 0
	v_cndmask_b32_e32 v124, v252, v124, vcc
	v_cmp_le_i32_e32 vcc, v57, v207
	v_add_u32_e32 v57, 0xffffff9e, v65
	s_nop 0
	v_cndmask_b32_e32 v108, v252, v108, vcc
	v_cmp_le_i32_e32 vcc, v57, v207
	v_add_u32_e32 v57, 0xffffffbe, v65
	s_nop 0
	v_cndmask_b32_e32 v125, v252, v125, vcc
	v_cmp_le_i32_e32 vcc, v57, v207
	v_add_u32_e32 v57, 0xffffff9f, v65
	s_nop 0
	v_cndmask_b32_e32 v109, v252, v109, vcc
	v_cmp_le_i32_e32 vcc, v57, v207
	v_add_u32_e32 v57, 0xffffffbf, v65
	s_nop 0
	v_cndmask_b32_e32 v126, v252, v126, vcc
	v_cmp_le_i32_e32 vcc, v57, v207
	v_add_u32_e32 v57, 0xffffffa0, v65
	s_nop 0
	v_cndmask_b32_e32 v110, v252, v110, vcc
	v_cmp_le_i32_e32 vcc, v57, v207
	v_subrev_u32_e32 v57, 64, v65
	s_nop 0
	v_cndmask_b32_e32 v127, v252, v127, vcc
	v_cmp_le_i32_e32 vcc, v57, v207
	s_nop 1
	v_cndmask_b32_e32 v111, v252, v111, vcc

.Lsqk_1b:
	s_add_i32 s33, s31, 2
	s_cmp_ge_u32 s33, s24
	s_cselect_b64 s[12:13], -1, 0
	s_and_b64 vcc, exec, s[12:13]
	s_cbranch_vccnz .LBB1_123
	s_add_i32 s2, s26, s22
	s_mov_b32 m0, s2
	s_nop 0
	global_load_lds_dwordx4 v211, s[6:7]
.LBB1_123:
	s_add_i32 s2, s26, 0x2000
	s_cmpk_lg_i32 s26, 0x4000
	s_cselect_b32 s25, s2, 0
	s_cmp_lt_u32 s31, s24
	s_cselect_b64 s[16:17], -1, 0
	s_cmp_ge_u32 s31, s24
	s_cbranch_scc1 .LBB1_125
	s_add_u32 s2, s4, 0x2000
	s_addc_u32 s3, s5, 0
	s_add_i32 s15, s25, s23
	s_mov_b32 m0, s15
	s_nop 0
	global_load_lds_dwordx4 v211, s[2:3]
